# MoE GEMMs: plain v_mfma_f32_16x16x128_f8f6f4 (fp8 e4m3 operands) instead of the MX-scaled form with unit scales -- same products, no scale operands
# speedup vs baseline: 1.0081x; 1.0049x over previous
.Lp9_na_done:
	v_add_u32_e32 v133, 0x10000, v169
	v_add_u32_e32 v142, 0x14000, v169
	ds_read_b128 v[134:137], v133
	ds_read_b128 v[138:141], v133 offset:1024
	ds_read_b128 v[176:179], v133 offset:2048
	ds_read_b128 v[180:183], v133 offset:3072
	ds_read_b128 v[184:187], v142
	ds_read_b128 v[188:191], v142 offset:1024
	ds_read_b128 v[192:195], v142 offset:2048
	ds_read_b128 v[196:199], v142 offset:3072
	s_add_i32 s70, s66, s68
	s_add_i32 s71, s68, 0xffffff80
	s_cmp_eq_u32 s67, 12
	s_cselect_b64 vcc, -1, 0
	s_and_b64 s[10:11], vcc, exec
	v_cndmask_b32_e32 v133, v129, v147, vcc
	s_cselect_b32 s69, 0, s68
	v_cndmask_b32_e32 v142, v131, v174, vcc
	v_cndmask_b32_e32 v143, v130, v173, vcc
	s_mov_b32 m0, s43
	ds_read_b128 v[200:203], v170
	ds_read_b128 v[204:207], v170 offset:1024
	ds_read_b128 v[208:211], v170 offset:2048
	ds_read_b128 v[212:215], v170 offset:3072
	ds_read_b128 v[216:219], v170 offset:4096
	ds_read_b128 v[220:223], v170 offset:5120
	ds_read_b128 v[224:227], v170 offset:6144
	ds_read_b128 v[228:231], v170 offset:7168
	buffer_load_dwordx4 v131, s[4:7], s71 offen lds
	s_mov_b32 m0, s44
	s_cselect_b32 s70, s23, s70
	buffer_load_dwordx4 v132, s[4:7], s71 offen lds
	s_waitcnt vmcnt(8)
	s_waitcnt lgkmcnt(0)
	s_barrier
	s_setprio 1
	s_nop 1
	s_waitcnt lgkmcnt(6)
	v_mfma_f32_16x16x128_f8f6f4 v[124:127], v[134:141], v[200:207], v[124:127]
	v_mfma_f32_16x16x128_f8f6f4 v[120:123], v[176:183], v[200:207], v[120:123]
	s_waitcnt lgkmcnt(4)
	v_mfma_f32_16x16x128_f8f6f4 v[108:111], v[134:141], v[208:215], v[108:111]
	v_mfma_f32_16x16x128_f8f6f4 v[104:107], v[176:183], v[208:215], v[104:107]
	s_waitcnt lgkmcnt(2)
	v_mfma_f32_16x16x128_f8f6f4 v[92:95], v[134:141], v[216:223], v[92:95]
	v_mfma_f32_16x16x128_f8f6f4 v[88:91], v[176:183], v[216:223], v[88:91]
	s_waitcnt lgkmcnt(0)
	v_mfma_f32_16x16x128_f8f6f4 v[76:79], v[134:141], v[224:231], v[76:79]
	v_mfma_f32_16x16x128_f8f6f4 v[72:75], v[176:183], v[224:231], v[72:75]
	s_setprio 0
	s_setprio 1
	s_nop 1
	v_mfma_f32_16x16x128_f8f6f4 v[116:119], v[184:191], v[200:207], v[116:119]
	v_mfma_f32_16x16x128_f8f6f4 v[112:115], v[192:199], v[200:207], v[112:115]
	v_mfma_f32_16x16x128_f8f6f4 v[100:103], v[184:191], v[208:215], v[100:103]
	v_mfma_f32_16x16x128_f8f6f4 v[96:99], v[192:199], v[208:215], v[96:99]
	v_mfma_f32_16x16x128_f8f6f4 v[84:87], v[184:191], v[216:223], v[84:87]
	v_mfma_f32_16x16x128_f8f6f4 v[80:83], v[192:199], v[216:223], v[80:83]
	v_mfma_f32_16x16x128_f8f6f4 v[68:71], v[184:191], v[224:231], v[68:71]
	v_mfma_f32_16x16x128_f8f6f4 v[64:67], v[192:199], v[224:231], v[64:67]
	s_setprio 0
	s_barrier
	s_mov_b32 m0, s26
	s_mov_b32 s10, s6
	s_mov_b32 s11, s7
	ds_read_b128 v[200:203], v170 offset:16384
	ds_read_b128 v[204:207], v170 offset:17408
	ds_read_b128 v[208:211], v170 offset:18432
	ds_read_b128 v[212:215], v170 offset:19456
	ds_read_b128 v[216:219], v170 offset:20480
	ds_read_b128 v[220:223], v170 offset:21504
	ds_read_b128 v[224:227], v170 offset:22528
	ds_read_b128 v[228:231], v170 offset:23552
	buffer_load_dwordx4 v157, s[8:11], s70 offen lds
	s_mov_b32 m0, s27
	s_add_i32 s71, s70, 0x40000
	buffer_load_dwordx4 v159, s[8:11], s70 offen lds
	s_mov_b32 m0, s28
	s_nop 0
	buffer_load_dwordx4 v157, s[8:11], s71 offen lds
	s_mov_b32 m0, s29
	s_nop 0
	buffer_load_dwordx4 v159, s[8:11], s71 offen lds
	s_mov_b32 m0, s25
	s_nop 0
	buffer_load_dwordx4 v133, s[4:7], s69 offen lds
	s_mov_b32 m0, s30
	s_nop 0
	buffer_load_dwordx4 v143, s[4:7], s69 offen lds
	s_waitcnt vmcnt(8)
	s_waitcnt lgkmcnt(0)
	s_barrier
	s_setprio 1
	s_nop 1
	s_waitcnt lgkmcnt(6)
	v_mfma_f32_16x16x128_f8f6f4 v[60:63], v[134:141], v[200:207], v[60:63]
	v_mfma_f32_16x16x128_f8f6f4 v[56:59], v[176:183], v[200:207], v[56:59]
	s_waitcnt lgkmcnt(4)
	v_mfma_f32_16x16x128_f8f6f4 v[44:47], v[134:141], v[208:215], v[44:47]
	v_mfma_f32_16x16x128_f8f6f4 v[40:43], v[176:183], v[208:215], v[40:43]
	s_waitcnt lgkmcnt(2)
	v_mfma_f32_16x16x128_f8f6f4 v[28:31], v[134:141], v[216:223], v[28:31]
	v_mfma_f32_16x16x128_f8f6f4 v[24:27], v[176:183], v[216:223], v[24:27]
	s_waitcnt lgkmcnt(0)
	v_mfma_f32_16x16x128_f8f6f4 v[12:15], v[134:141], v[224:231], v[12:15]
	v_mfma_f32_16x16x128_f8f6f4 v[8:11], v[176:183], v[224:231], v[8:11]
	s_setprio 0
	s_setprio 1
	s_nop 1
	v_mfma_f32_16x16x128_f8f6f4 v[52:55], v[184:191], v[200:207], v[52:55]
	v_mfma_f32_16x16x128_f8f6f4 v[48:51], v[192:199], v[200:207], v[48:51]
	v_mfma_f32_16x16x128_f8f6f4 v[36:39], v[184:191], v[208:215], v[36:39]
	v_mfma_f32_16x16x128_f8f6f4 v[32:35], v[192:199], v[208:215], v[32:35]
	v_mfma_f32_16x16x128_f8f6f4 v[20:23], v[184:191], v[216:223], v[20:23]
	v_mfma_f32_16x16x128_f8f6f4 v[16:19], v[192:199], v[216:223], v[16:19]
	v_mfma_f32_16x16x128_f8f6f4 v[4:7], v[184:191], v[224:231], v[4:7]
	v_mfma_f32_16x16x128_f8f6f4 v[0:3], v[192:199], v[224:231], v[0:3]
	s_setprio 0
	s_barrier
	v_add_u32_e32 v144, 0x18000, v169
	ds_read_b128 v[134:137], v144
	ds_read_b128 v[138:141], v144 offset:1024
	ds_read_b128 v[176:179], v144 offset:2048
	ds_read_b128 v[180:183], v144 offset:3072
	v_add_u32_e32 v144, 0x1c000, v169
	ds_read_b128 v[184:187], v144
	ds_read_b128 v[188:191], v144 offset:1024
	ds_read_b128 v[192:195], v144 offset:2048
	ds_read_b128 v[196:199], v144 offset:3072
	s_mov_b32 m0, s31
	ds_read_b128 v[200:203], v170 offset:32768
	ds_read_b128 v[204:207], v170 offset:33792
	ds_read_b128 v[208:211], v170 offset:34816
	ds_read_b128 v[212:215], v170 offset:35840
	ds_read_b128 v[216:219], v170 offset:36864
	ds_read_b128 v[220:223], v170 offset:37888
	ds_read_b128 v[224:227], v170 offset:38912
	ds_read_b128 v[228:231], v170 offset:39936
	v_cndmask_b32_e32 v144, v132, v175, vcc
	buffer_load_dwordx4 v142, s[4:7], s69 offen lds
	s_mov_b32 m0, s33
	s_nop 0
	buffer_load_dwordx4 v144, s[4:7], s69 offen lds
	s_waitcnt vmcnt(8)
	s_waitcnt lgkmcnt(0)
	s_barrier
	s_setprio 1
	s_nop 1
	s_waitcnt lgkmcnt(6)
	v_mfma_f32_16x16x128_f8f6f4 v[124:127], v[134:141], v[200:207], v[124:127]
	v_mfma_f32_16x16x128_f8f6f4 v[120:123], v[176:183], v[200:207], v[120:123]
	s_waitcnt lgkmcnt(4)
	v_mfma_f32_16x16x128_f8f6f4 v[108:111], v[134:141], v[208:215], v[108:111]
	v_mfma_f32_16x16x128_f8f6f4 v[104:107], v[176:183], v[208:215], v[104:107]
	s_waitcnt lgkmcnt(2)
	v_mfma_f32_16x16x128_f8f6f4 v[92:95], v[134:141], v[216:223], v[92:95]
	v_mfma_f32_16x16x128_f8f6f4 v[88:91], v[176:183], v[216:223], v[88:91]
	s_waitcnt lgkmcnt(0)
	v_mfma_f32_16x16x128_f8f6f4 v[76:79], v[134:141], v[224:231], v[76:79]
	v_mfma_f32_16x16x128_f8f6f4 v[72:75], v[176:183], v[224:231], v[72:75]
	s_setprio 0
	s_setprio 1
	s_nop 1
	v_mfma_f32_16x16x128_f8f6f4 v[116:119], v[184:191], v[200:207], v[116:119]
	v_mfma_f32_16x16x128_f8f6f4 v[112:115], v[192:199], v[200:207], v[112:115]
	v_mfma_f32_16x16x128_f8f6f4 v[100:103], v[184:191], v[208:215], v[100:103]
	v_mfma_f32_16x16x128_f8f6f4 v[96:99], v[192:199], v[208:215], v[96:99]
	v_mfma_f32_16x16x128_f8f6f4 v[84:87], v[184:191], v[216:223], v[84:87]
	v_mfma_f32_16x16x128_f8f6f4 v[80:83], v[192:199], v[216:223], v[80:83]
	v_mfma_f32_16x16x128_f8f6f4 v[68:71], v[184:191], v[224:231], v[68:71]
	v_mfma_f32_16x16x128_f8f6f4 v[64:67], v[192:199], v[224:231], v[64:67]
	s_setprio 0
	s_barrier
	s_mov_b32 m0, s35
	s_add_i32 s71, s70, 0x80
	ds_read_b128 v[200:203], v170 offset:49152
	ds_read_b128 v[204:207], v170 offset:50176
	ds_read_b128 v[208:211], v170 offset:51200
	ds_read_b128 v[212:215], v170 offset:52224
	ds_read_b128 v[216:219], v170 offset:53248
	ds_read_b128 v[220:223], v170 offset:54272
	ds_read_b128 v[224:227], v170 offset:55296
	ds_read_b128 v[228:231], v170 offset:56320
	buffer_load_dwordx4 v157, s[8:11], s71 offen lds
	s_mov_b32 m0, s36
	s_add_i32 s70, s70, 0x40080
	buffer_load_dwordx4 v159, s[8:11], s71 offen lds
	s_mov_b32 m0, s41
	s_bitset1_b32 s69, 7
	buffer_load_dwordx4 v157, s[8:11], s70 offen lds
	s_mov_b32 m0, s42
	s_nop 0
	buffer_load_dwordx4 v159, s[8:11], s70 offen lds
	s_mov_b32 m0, s37
	s_nop 0
	buffer_load_dwordx4 v133, s[4:7], s69 offen lds
	s_mov_b32 m0, s40
	s_nop 0
	buffer_load_dwordx4 v143, s[4:7], s69 offen lds
	s_waitcnt vmcnt(8)
	s_waitcnt lgkmcnt(0)
	s_barrier
	s_setprio 1
	s_nop 1
	s_waitcnt lgkmcnt(6)
	v_mfma_f32_16x16x128_f8f6f4 v[60:63], v[134:141], v[200:207], v[60:63]
	v_mfma_f32_16x16x128_f8f6f4 v[56:59], v[176:183], v[200:207], v[56:59]
	s_waitcnt lgkmcnt(4)
	v_mfma_f32_16x16x128_f8f6f4 v[44:47], v[134:141], v[208:215], v[44:47]
	v_mfma_f32_16x16x128_f8f6f4 v[40:43], v[176:183], v[208:215], v[40:43]
	s_waitcnt lgkmcnt(2)
	v_mfma_f32_16x16x128_f8f6f4 v[28:31], v[134:141], v[216:223], v[28:31]
	v_mfma_f32_16x16x128_f8f6f4 v[24:27], v[176:183], v[216:223], v[24:27]
	s_waitcnt lgkmcnt(0)
	v_mfma_f32_16x16x128_f8f6f4 v[12:15], v[134:141], v[224:231], v[12:15]
	v_mfma_f32_16x16x128_f8f6f4 v[8:11], v[176:183], v[224:231], v[8:11]
	s_setprio 0
	s_setprio 1
	s_nop 1
	v_mfma_f32_16x16x128_f8f6f4 v[52:55], v[184:191], v[200:207], v[52:55]
	v_mfma_f32_16x16x128_f8f6f4 v[48:51], v[192:199], v[200:207], v[48:51]
	v_mfma_f32_16x16x128_f8f6f4 v[36:39], v[184:191], v[208:215], v[36:39]
	v_mfma_f32_16x16x128_f8f6f4 v[32:35], v[192:199], v[208:215], v[32:35]
	v_mfma_f32_16x16x128_f8f6f4 v[20:23], v[184:191], v[216:223], v[20:23]
	v_mfma_f32_16x16x128_f8f6f4 v[16:19], v[192:199], v[216:223], v[16:19]
	v_mfma_f32_16x16x128_f8f6f4 v[4:7], v[184:191], v[224:231], v[4:7]
	v_mfma_f32_16x16x128_f8f6f4 v[0:3], v[192:199], v[224:231], v[0:3]
	s_setprio 0
	s_barrier
	s_add_i32 s67, s67, 2
	s_addk_i32 s68, 0x100
	s_cmp_gt_u32 s67, 13
	s_cbranch_scc0 .LBB0_1157
	s_and_b64 vcc, exec, s[18:19]
	s_cbranch_vccz .LBB0_1160
	s_barrier

.LBB0_1254:
	v_add_u32_e32 v140, 0x10000, v177
	v_add_u32_e32 v141, 0x14000, v177
	ds_read_b128 v[132:135], v140
	ds_read_b128 v[136:139], v140 offset:1024
	ds_read_b128 v[186:189], v140 offset:2048
	ds_read_b128 v[190:193], v140 offset:3072
	ds_read_b128 v[194:197], v141
	ds_read_b128 v[198:201], v141 offset:1024
	ds_read_b128 v[202:205], v141 offset:2048
	ds_read_b128 v[206:209], v141 offset:3072
	s_add_i32 s10, s6, s5
	s_add_i32 s11, s5, 0xffffff80
	s_cmp_eq_u32 s4, 12
	s_cselect_b64 vcc, -1, 0
	s_and_b64 s[8:9], vcc, exec
	v_cndmask_b32_e32 v140, v128, v182, vcc
	s_cselect_b32 s7, 0, s5
	v_cndmask_b32_e32 v141, v130, v184, vcc
	v_cndmask_b32_e32 v142, v129, v183, vcc
	s_mov_b32 m0, s57
	ds_read_b128 v[210:213], v178
	ds_read_b128 v[214:217], v178 offset:1024
	ds_read_b128 v[218:221], v178 offset:2048
	ds_read_b128 v[222:225], v178 offset:3072
	ds_read_b128 v[226:229], v178 offset:4096
	ds_read_b128 v[230:233], v178 offset:5120
	ds_read_b128 v[234:237], v178 offset:6144
	ds_read_b128 v[238:241], v178 offset:7168
	buffer_load_dwordx4 v130, s[20:23], s11 offen lds
	s_mov_b32 m0, s58
	s_cselect_b32 s8, s80, s10
	buffer_load_dwordx4 v131, s[20:23], s11 offen lds
	s_waitcnt vmcnt(8)
	s_waitcnt lgkmcnt(0)
	s_barrier
	s_setprio 1
	s_nop 1
	s_waitcnt lgkmcnt(6)
	v_mfma_f32_16x16x128_f8f6f4 v[124:127], v[132:139], v[210:217], v[124:127]
	v_mfma_f32_16x16x128_f8f6f4 v[120:123], v[186:193], v[210:217], v[120:123]
	s_waitcnt lgkmcnt(4)
	v_mfma_f32_16x16x128_f8f6f4 v[108:111], v[132:139], v[218:225], v[108:111]
	v_mfma_f32_16x16x128_f8f6f4 v[104:107], v[186:193], v[218:225], v[104:107]
	s_waitcnt lgkmcnt(2)
	v_mfma_f32_16x16x128_f8f6f4 v[92:95], v[132:139], v[226:233], v[92:95]
	v_mfma_f32_16x16x128_f8f6f4 v[88:91], v[186:193], v[226:233], v[88:91]
	s_waitcnt lgkmcnt(0)
	v_mfma_f32_16x16x128_f8f6f4 v[76:79], v[132:139], v[234:241], v[76:79]
	v_mfma_f32_16x16x128_f8f6f4 v[72:75], v[186:193], v[234:241], v[72:75]
	s_setprio 0
	s_setprio 1
	s_nop 1
	v_mfma_f32_16x16x128_f8f6f4 v[116:119], v[194:201], v[210:217], v[116:119]
	v_mfma_f32_16x16x128_f8f6f4 v[112:115], v[202:209], v[210:217], v[112:115]
	v_mfma_f32_16x16x128_f8f6f4 v[100:103], v[194:201], v[218:225], v[100:103]
	v_mfma_f32_16x16x128_f8f6f4 v[96:99], v[202:209], v[218:225], v[96:99]
	v_mfma_f32_16x16x128_f8f6f4 v[84:87], v[194:201], v[226:233], v[84:87]
	v_mfma_f32_16x16x128_f8f6f4 v[80:83], v[202:209], v[226:233], v[80:83]
	v_mfma_f32_16x16x128_f8f6f4 v[68:71], v[194:201], v[234:241], v[68:71]
	v_mfma_f32_16x16x128_f8f6f4 v[64:67], v[202:209], v[234:241], v[64:67]
	s_setprio 0
	s_barrier
	s_mov_b32 m0, s43
	s_mov_b32 s26, s22
	s_mov_b32 s27, s23
	ds_read_b128 v[210:213], v178 offset:16384
	ds_read_b128 v[214:217], v178 offset:17408
	ds_read_b128 v[218:221], v178 offset:18432
	ds_read_b128 v[222:225], v178 offset:19456
	ds_read_b128 v[226:229], v178 offset:20480
	ds_read_b128 v[230:233], v178 offset:21504
	ds_read_b128 v[234:237], v178 offset:22528
	ds_read_b128 v[238:241], v178 offset:23552
	buffer_load_dwordx4 v155, s[24:27], s8 offen lds
	s_mov_b32 m0, s44
	s_add_i32 s9, s8, 0x40000
	buffer_load_dwordx4 v161, s[24:27], s8 offen lds
	s_mov_b32 m0, s45
	s_nop 0
	buffer_load_dwordx4 v155, s[24:27], s9 offen lds
	s_mov_b32 m0, s46
	s_nop 0
	buffer_load_dwordx4 v161, s[24:27], s9 offen lds
	s_mov_b32 m0, s42
	s_nop 0
	buffer_load_dwordx4 v140, s[20:23], s7 offen lds
	s_mov_b32 m0, s47
	s_nop 0
	buffer_load_dwordx4 v142, s[20:23], s7 offen lds
	s_waitcnt vmcnt(8)
	s_waitcnt lgkmcnt(0)
	s_barrier
	s_setprio 1
	s_nop 1
	s_waitcnt lgkmcnt(6)
	v_mfma_f32_16x16x128_f8f6f4 v[60:63], v[132:139], v[210:217], v[60:63]
	v_mfma_f32_16x16x128_f8f6f4 v[56:59], v[186:193], v[210:217], v[56:59]
	s_waitcnt lgkmcnt(4)
	v_mfma_f32_16x16x128_f8f6f4 v[44:47], v[132:139], v[218:225], v[44:47]
	v_mfma_f32_16x16x128_f8f6f4 v[40:43], v[186:193], v[218:225], v[40:43]
	s_waitcnt lgkmcnt(2)
	v_mfma_f32_16x16x128_f8f6f4 v[28:31], v[132:139], v[226:233], v[28:31]
	v_mfma_f32_16x16x128_f8f6f4 v[24:27], v[186:193], v[226:233], v[24:27]
	s_waitcnt lgkmcnt(0)
	v_mfma_f32_16x16x128_f8f6f4 v[12:15], v[132:139], v[234:241], v[12:15]
	v_mfma_f32_16x16x128_f8f6f4 v[8:11], v[186:193], v[234:241], v[8:11]
	s_setprio 0
	s_setprio 1
	s_nop 1
	v_mfma_f32_16x16x128_f8f6f4 v[52:55], v[194:201], v[210:217], v[52:55]
	v_mfma_f32_16x16x128_f8f6f4 v[48:51], v[202:209], v[210:217], v[48:51]
	v_mfma_f32_16x16x128_f8f6f4 v[36:39], v[194:201], v[218:225], v[36:39]
	v_mfma_f32_16x16x128_f8f6f4 v[32:35], v[202:209], v[218:225], v[32:35]
	v_mfma_f32_16x16x128_f8f6f4 v[20:23], v[194:201], v[226:233], v[20:23]
	v_mfma_f32_16x16x128_f8f6f4 v[16:19], v[202:209], v[226:233], v[16:19]
	v_mfma_f32_16x16x128_f8f6f4 v[4:7], v[194:201], v[234:241], v[4:7]
	v_mfma_f32_16x16x128_f8f6f4 v[0:3], v[202:209], v[234:241], v[0:3]
	s_setprio 0
	s_barrier
	v_add_u32_e32 v143, 0x18000, v177
	ds_read_b128 v[132:135], v143
	ds_read_b128 v[136:139], v143 offset:1024
	ds_read_b128 v[186:189], v143 offset:2048
	ds_read_b128 v[190:193], v143 offset:3072
	v_add_u32_e32 v143, 0x1c000, v177
	ds_read_b128 v[194:197], v143
	ds_read_b128 v[198:201], v143 offset:1024
	ds_read_b128 v[202:205], v143 offset:2048
	ds_read_b128 v[206:209], v143 offset:3072
	s_mov_b32 m0, s48
	ds_read_b128 v[210:213], v178 offset:32768
	ds_read_b128 v[214:217], v178 offset:33792
	ds_read_b128 v[218:221], v178 offset:34816
	ds_read_b128 v[222:225], v178 offset:35840
	ds_read_b128 v[226:229], v178 offset:36864
	ds_read_b128 v[230:233], v178 offset:37888
	ds_read_b128 v[234:237], v178 offset:38912
	ds_read_b128 v[238:241], v178 offset:39936
	v_cndmask_b32_e32 v143, v131, v185, vcc
	buffer_load_dwordx4 v141, s[20:23], s7 offen lds
	s_mov_b32 m0, s49
	s_nop 0
	buffer_load_dwordx4 v143, s[20:23], s7 offen lds
	s_waitcnt vmcnt(8)
	s_waitcnt lgkmcnt(0)
	s_barrier
	s_setprio 1
	s_nop 1
	s_waitcnt lgkmcnt(6)
	v_mfma_f32_16x16x128_f8f6f4 v[124:127], v[132:139], v[210:217], v[124:127]
	v_mfma_f32_16x16x128_f8f6f4 v[120:123], v[186:193], v[210:217], v[120:123]
	s_waitcnt lgkmcnt(4)
	v_mfma_f32_16x16x128_f8f6f4 v[108:111], v[132:139], v[218:225], v[108:111]
	v_mfma_f32_16x16x128_f8f6f4 v[104:107], v[186:193], v[218:225], v[104:107]
	s_waitcnt lgkmcnt(2)
	v_mfma_f32_16x16x128_f8f6f4 v[92:95], v[132:139], v[226:233], v[92:95]
	v_mfma_f32_16x16x128_f8f6f4 v[88:91], v[186:193], v[226:233], v[88:91]
	s_waitcnt lgkmcnt(0)
	v_mfma_f32_16x16x128_f8f6f4 v[76:79], v[132:139], v[234:241], v[76:79]
	v_mfma_f32_16x16x128_f8f6f4 v[72:75], v[186:193], v[234:241], v[72:75]
	s_setprio 0
	s_setprio 1
	s_nop 1
	v_mfma_f32_16x16x128_f8f6f4 v[116:119], v[194:201], v[210:217], v[116:119]
	v_mfma_f32_16x16x128_f8f6f4 v[112:115], v[202:209], v[210:217], v[112:115]
	v_mfma_f32_16x16x128_f8f6f4 v[100:103], v[194:201], v[218:225], v[100:103]
	v_mfma_f32_16x16x128_f8f6f4 v[96:99], v[202:209], v[218:225], v[96:99]
	v_mfma_f32_16x16x128_f8f6f4 v[84:87], v[194:201], v[226:233], v[84:87]
	v_mfma_f32_16x16x128_f8f6f4 v[80:83], v[202:209], v[226:233], v[80:83]
	v_mfma_f32_16x16x128_f8f6f4 v[68:71], v[194:201], v[234:241], v[68:71]
	v_mfma_f32_16x16x128_f8f6f4 v[64:67], v[202:209], v[234:241], v[64:67]
	s_setprio 0
	s_barrier
	s_mov_b32 m0, s51
	s_add_i32 s9, s8, 0x80
	ds_read_b128 v[210:213], v178 offset:49152
	ds_read_b128 v[214:217], v178 offset:50176
	ds_read_b128 v[218:221], v178 offset:51200
	ds_read_b128 v[222:225], v178 offset:52224
	ds_read_b128 v[226:229], v178 offset:53248
	ds_read_b128 v[230:233], v178 offset:54272
	ds_read_b128 v[234:237], v178 offset:55296
	ds_read_b128 v[238:241], v178 offset:56320
	buffer_load_dwordx4 v155, s[24:27], s9 offen lds
	s_mov_b32 m0, s52
	s_add_i32 s8, s8, 0x40080
	buffer_load_dwordx4 v161, s[24:27], s9 offen lds
	s_mov_b32 m0, s55
	s_bitset1_b32 s7, 7
	buffer_load_dwordx4 v155, s[24:27], s8 offen lds
	s_mov_b32 m0, s56
	s_nop 0
	buffer_load_dwordx4 v161, s[24:27], s8 offen lds
	s_mov_b32 m0, s53
	s_nop 0
	buffer_load_dwordx4 v140, s[20:23], s7 offen lds
	s_mov_b32 m0, s54
	s_nop 0
	buffer_load_dwordx4 v142, s[20:23], s7 offen lds
	s_waitcnt vmcnt(8)
	s_waitcnt lgkmcnt(0)
	s_barrier
	s_setprio 1
	s_nop 1
	s_waitcnt lgkmcnt(6)
	v_mfma_f32_16x16x128_f8f6f4 v[60:63], v[132:139], v[210:217], v[60:63]
	v_mfma_f32_16x16x128_f8f6f4 v[56:59], v[186:193], v[210:217], v[56:59]
	s_waitcnt lgkmcnt(4)
	v_mfma_f32_16x16x128_f8f6f4 v[44:47], v[132:139], v[218:225], v[44:47]
	v_mfma_f32_16x16x128_f8f6f4 v[40:43], v[186:193], v[218:225], v[40:43]
	s_waitcnt lgkmcnt(2)
	v_mfma_f32_16x16x128_f8f6f4 v[28:31], v[132:139], v[226:233], v[28:31]
	v_mfma_f32_16x16x128_f8f6f4 v[24:27], v[186:193], v[226:233], v[24:27]
	s_waitcnt lgkmcnt(0)
	v_mfma_f32_16x16x128_f8f6f4 v[12:15], v[132:139], v[234:241], v[12:15]
	v_mfma_f32_16x16x128_f8f6f4 v[8:11], v[186:193], v[234:241], v[8:11]
	s_setprio 0
	s_setprio 1
	s_nop 1
	v_mfma_f32_16x16x128_f8f6f4 v[52:55], v[194:201], v[210:217], v[52:55]
	v_mfma_f32_16x16x128_f8f6f4 v[48:51], v[202:209], v[210:217], v[48:51]
	v_mfma_f32_16x16x128_f8f6f4 v[36:39], v[194:201], v[218:225], v[36:39]
	v_mfma_f32_16x16x128_f8f6f4 v[32:35], v[202:209], v[218:225], v[32:35]
	v_mfma_f32_16x16x128_f8f6f4 v[20:23], v[194:201], v[226:233], v[20:23]
	v_mfma_f32_16x16x128_f8f6f4 v[16:19], v[202:209], v[226:233], v[16:19]
	v_mfma_f32_16x16x128_f8f6f4 v[4:7], v[194:201], v[234:241], v[4:7]
	v_mfma_f32_16x16x128_f8f6f4 v[0:3], v[202:209], v[234:241], v[0:3]
	s_setprio 0
	s_barrier
	s_add_i32 s4, s4, 2
	s_addk_i32 s5, 0x100
	s_cmp_gt_u32 s4, 13
	s_cbranch_scc0 .LBB0_1254
	s_and_b64 vcc, exec, s[38:39]
	s_cbranch_vccz .LBB0_1257
	s_barrier
